# attention: static s_setprio 1 for waves 4-7
# baseline (speedup 1.0000x reference)
.LBB0_626:
	s_or_b64 exec, exec, s[30:31]
	v_readlane_b32 s0, v255, 32
	v_readlane_b32 s1, v255, 33
	s_cmp_eq_u32 s0, 3
	s_cselect_b64 s[2:3], -1, 0
	s_cmp_lg_u32 s0, 3
	v_readlane_b32 s0, v252, 18
	v_writelane_b32 v255, s2, 37
	v_readlane_b32 s1, v252, 19
	s_cselect_b64 s[58:59], -1, 0
	v_writelane_b32 v255, s3, 38
	s_andn2_b64 vcc, exec, s[0:1]
	s_mov_b64 s[0:1], -1
	s_waitcnt lgkmcnt(0)
	s_barrier
	s_cbranch_vccnz .LBB0_676
	s_mov_b32 s101, 0
	v_readfirstlane_b32 s100, v0
	s_nop 0
	s_lshr_b32 s100, s100, 8
	s_cmp_lg_u32 s100, 0
	s_cbranch_scc0 .Lattn_noprio
	s_setprio 1
.Lattn_noprio:
	v_readlane_b32 s0, v255, 37
	v_readlane_b32 s1, v255, 38
	s_and_b64 s[0:1], s[0:1], exec
	s_movk_i32 s0, 0x240
	s_cselect_b32 s16, 0x200, s0
	v_readlane_b32 s0, v252, 29
	s_cmp_lt_u32 s0, s16
	v_mov_b32_e32 v2, v0
	s_cbranch_scc0 .LBB0_672
	v_lshlrev_b32_e32 v3, 3, v2
	v_and_b32_e32 v4, 63, v2
	v_ashrrev_i32_e32 v159, 7, v2
	v_ashrrev_i32_e32 v156, 3, v2
	v_and_b32_e32 v158, 56, v3
	v_and_b32_e32 v3, 31, v2
	v_bfe_u32 v5, v2, 5, 1
	v_lshrrev_b32_e32 v2, 1, v2
	s_movk_i32 s0, 0x90
	v_cmp_gt_u32_e64 s[2:3], 32, v4
	v_mov_b32_e32 v4, 0x1200
	v_mov_b32_e32 v130, v131
	v_mov_b32_e32 v36, v131
	v_mov_b32_e32 v37, v131
	v_and_or_b32 v160, v2, 32, v3
	v_mul_lo_u32 v163, v156, s0
	v_lshlrev_b32_e32 v2, 2, v5
	v_mad_u32_u24 v176, v3, s0, v4
	s_movk_i32 s0, 0x88
	v_mov_b32_e32 v4, 0x1100
	v_mov_b32_e32 v132, v131
	v_mov_b32_e32 v133, v131
	v_mov_b32_e32 v34, v131
	v_mov_b32_e32 v35, v131
	v_mov_b64_e32 v[38:39], v[130:131]
	v_mov_b64_e32 v[68:69], v[36:37]
	v_mov_b64_e32 v[78:79], v[130:131]
	v_mov_b64_e32 v[92:93], v[36:37]
	v_mov_b64_e32 v[94:95], v[130:131]
	v_lshlrev_b32_e32 v162, 3, v5
	v_ashrrev_i32_e32 v157, 31, v156
	v_lshlrev_b32_e32 v161, 6, v159
	s_waitcnt vmcnt(0)
	v_lshlrev_b32_e32 v170, 4, v5
	v_or_b32_e32 v171, 0xffffff80, v2
	v_or_b32_e32 v172, 0xffffff80, v160
	v_or_b32_e32 v173, 0x80, v160
	v_mul_u32_u24_e32 v174, 0x88, v158
	v_mul_u32_u24_e32 v175, 0x90, v3
	v_mul_u32_u24_e32 v177, 0x88, v3
	v_mad_u32_u24 v178, v3, s0, v4
	s_mov_b64 s[6:7], -1
	v_lshlrev_b32_e32 v164, 1, v2
	v_mov_b64_e32 v[40:41], v[132:133]
	v_mov_b64_e32 v[66:67], v[34:35]
	v_mov_b64_e32 v[80:81], v[132:133]
	v_mov_b64_e32 v[90:91], v[34:35]
	v_mov_b64_e32 v[96:97], v[132:133]
	v_readlane_b32 s8, v252, 29
	s_branch .LBB0_631

.LBB0_672:
	s_setprio 0
	v_mov_b32_e32 v2, v0
	v_readlane_b32 s0, v252, 32
	v_readlane_b32 s1, v252, 33
	v_ashrrev_i32_e32 v3, 31, v2
	s_nop 0
	v_lshl_add_u64 v[6:7], s[0:1], 0, v[2:3]
	s_mov_b64 s[0:1], 0x2000
	v_cmp_gt_i64_e32 vcc, s[0:1], v[6:7]
	s_and_saveexec_b64 s[0:1], vcc
	v_readlane_b32 s6, v252, 25
	v_readlane_b32 s8, v252, 27
	v_readlane_b32 s7, v252, 26
	v_readlane_b32 s9, v252, 28
	s_mov_b64 s[10:11], 0x80000
	s_cbranch_execz .LBB0_675
	v_readlane_b32 s2, v252, 34
	v_readlane_b32 s3, v252, 35
	s_nop 1
	v_lshl_add_u64 v[2:3], v[6:7], 2, s[2:3]
	s_mov_b64 s[2:3], 0
